# epilogue stores of MoE-down, gate_up and in_proj part 0: packed outputs exchanged between lanes with ds_bpermute so 4 adjacent lanes write one contiguous 32/64-byte piece of a row
# speedup vs baseline: 1.0392x; 1.0081x over previous
.LBB0_581:
	s_mov_b32 s11, -1
	v_pk_mul_f32 v[126:127], v[126:127], s[86:87] op_sel_hi:[1,0]
	v_mbcnt_lo_u32_b32 v0, s11, 0
	v_mbcnt_hi_u32_b32 v0, s11, v0
	s_lshl_b32 s11, s16, 8
	s_add_i32 s11, s11, s41
	v_and_or_b32 v130, v0, 15, s11
	v_and_b32_e32 v231, 3, v0
	v_lshrrev_b32_e32 v232, 2, v0
	v_lshlrev_b32_e32 v233, 4, v231
	v_or_b32_e32 v233, v233, v232
	v_lshlrev_b32_e32 v233, 2, v233
	v_or_b32_e32 v234, s11, v232
	s_mov_b32 s99, 0
	s_lshl_b32 s11, s53, 8
	v_lshrrev_b32_e32 v0, 1, v0
	v_and_or_b32 v0, v0, 24, s11
	v_or_b32_e32 v138, s42, v0
	v_lshlrev_b32_e32 v235, 3, v231
	v_or_b32_e32 v235, s11, v235
	v_or_b32_e32 v235, s42, v235
	v_mov_b32_e32 v237, 0
	v_mov_b32_e32 v236, v234
	v_lshlrev_b64 v[236:237], 16, v[236:237]
	v_lshl_add_u64 v[236:237], s[6:7], 0, v[236:237]
	v_lshlrev_b32_e32 v238, 1, v235
	v_mov_b32_e32 v239, 0
	v_lshl_add_u64 v[236:237], v[236:237], 0, v[238:239]
	v_ashrrev_i32_e32 v131, 31, v130
	v_lshlrev_b64 v[140:141], 16, v[130:131]
	v_pk_mul_f32 v[122:123], v[122:123], s[86:87] op_sel_hi:[1,0]
	v_ashrrev_i32_e32 v139, 31, v138
	v_lshl_add_u64 v[140:141], s[6:7], 0, v[140:141]
	v_pk_mul_f32 v[128:129], v[128:129], s[86:87] op_sel_hi:[1,0]
	v_pk_mul_f32 v[142:143], v[124:125], s[86:87] op_sel_hi:[1,0]
	v_cvt_pk_bf16_f32 v124, v126, v127
	v_cvt_pk_bf16_f32 v126, v122, v123
	v_lshlrev_b64 v[122:123], 1, v[138:139]
	v_cvt_pk_bf16_f32 v125, v128, v129
	v_cvt_pk_bf16_f32 v127, v142, v143
	v_lshl_add_u64 v[128:129], v[140:141], 0, v[122:123]
	ds_bpermute_b32 v200, v233, v124
	ds_bpermute_b32 v201, v233, v125
	ds_bpermute_b32 v202, v233, v126
	ds_bpermute_b32 v203, v233, v127
	s_mov_b32 s98, 0x0
	v_lshl_add_u64 v[212:213], v[236:237], 0, s[98:99]
	v_pk_mul_f32 v[116:117], v[116:117], s[86:87] op_sel_hi:[1,0]
	v_pk_mul_f32 v[114:115], v[114:115], s[86:87] op_sel_hi:[1,0]
	v_pk_mul_f32 v[124:125], v[108:109], s[86:87] op_sel_hi:[1,0]
	v_pk_mul_f32 v[108:109], v[106:107], s[86:87] op_sel_hi:[1,0]
	v_cvt_pk_bf16_f32 v106, v114, v115
	v_cvt_pk_bf16_f32 v107, v116, v117
	v_cvt_pk_bf16_f32 v108, v108, v109
	v_cvt_pk_bf16_f32 v109, v124, v125
	ds_bpermute_b32 v204, v233, v106
	ds_bpermute_b32 v205, v233, v107
	ds_bpermute_b32 v206, v233, v108
	ds_bpermute_b32 v207, v233, v109
	s_mov_b32 s98, 0x0
	v_lshl_add_u64 v[214:215], v[236:237], 0, s[98:99]
	s_waitcnt lgkmcnt(4)
	global_store_dwordx4 v[212:213], v[200:203], off
	v_pk_mul_f32 v[112:113], v[112:113], s[86:87] op_sel_hi:[1,0]
	v_pk_mul_f32 v[110:111], v[110:111], s[86:87] op_sel_hi:[1,0]
	v_or_b32_e32 v106, 16, v130
	v_ashrrev_i32_e32 v107, 31, v106
	v_lshlrev_b64 v[106:107], 16, v[106:107]
	v_lshl_add_u64 v[114:115], s[6:7], 0, v[106:107]
	v_pk_mul_f32 v[108:109], v[120:121], s[86:87] op_sel_hi:[1,0]
	v_pk_mul_f32 v[106:107], v[118:119], s[86:87] op_sel_hi:[1,0]
	v_pk_mul_f32 v[100:101], v[100:101], s[86:87] op_sel_hi:[1,0]
	v_cvt_pk_bf16_f32 v106, v106, v107
	v_cvt_pk_bf16_f32 v107, v108, v109
	v_cvt_pk_bf16_f32 v108, v110, v111
	v_cvt_pk_bf16_f32 v109, v112, v113
	v_lshl_add_u64 v[110:111], v[114:115], 0, v[122:123]
	ds_bpermute_b32 v208, v233, v106
	ds_bpermute_b32 v209, v233, v107
	ds_bpermute_b32 v210, v233, v108
	ds_bpermute_b32 v211, v233, v109
	s_mov_b32 s98, 0x100000
	v_lshl_add_u64 v[216:217], v[236:237], 0, s[98:99]
	s_waitcnt lgkmcnt(4)
	global_store_dwordx4 v[214:215], v[204:207], off offset:256
	v_pk_mul_f32 v[98:99], v[98:99], s[86:87] op_sel_hi:[1,0]
	v_pk_mul_f32 v[96:97], v[96:97], s[86:87] op_sel_hi:[1,0]
	v_pk_mul_f32 v[106:107], v[92:93], s[86:87] op_sel_hi:[1,0]
	v_pk_mul_f32 v[92:93], v[90:91], s[86:87] op_sel_hi:[1,0]
	v_cvt_pk_bf16_f32 v90, v98, v99
	v_cvt_pk_bf16_f32 v91, v100, v101
	v_cvt_pk_bf16_f32 v92, v92, v93
	v_cvt_pk_bf16_f32 v93, v106, v107
	ds_bpermute_b32 v200, v233, v90
	ds_bpermute_b32 v201, v233, v91
	ds_bpermute_b32 v202, v233, v92
	ds_bpermute_b32 v203, v233, v93
	s_mov_b32 s98, 0x100000
	v_lshl_add_u64 v[212:213], v[236:237], 0, s[98:99]
	s_waitcnt lgkmcnt(4)
	global_store_dwordx4 v[216:217], v[208:211], off
	v_pk_mul_f32 v[94:95], v[94:95], s[86:87] op_sel_hi:[1,0]
	v_pk_mul_f32 v[84:85], v[84:85], s[86:87] op_sel_hi:[1,0]
	v_or_b32_e32 v90, 32, v130
	v_ashrrev_i32_e32 v91, 31, v90
	v_lshlrev_b64 v[90:91], 16, v[90:91]
	v_lshl_add_u64 v[98:99], s[6:7], 0, v[90:91]
	v_pk_mul_f32 v[92:93], v[104:105], s[86:87] op_sel_hi:[1,0]
	v_pk_mul_f32 v[90:91], v[102:103], s[86:87] op_sel_hi:[1,0]
	v_pk_mul_f32 v[82:83], v[82:83], s[86:87] op_sel_hi:[1,0]
	v_cvt_pk_bf16_f32 v90, v90, v91
	v_cvt_pk_bf16_f32 v91, v92, v93
	v_cvt_pk_bf16_f32 v92, v94, v95
	v_cvt_pk_bf16_f32 v93, v96, v97
	v_lshl_add_u64 v[94:95], v[98:99], 0, v[122:123]
	ds_bpermute_b32 v204, v233, v90
	ds_bpermute_b32 v205, v233, v91
	ds_bpermute_b32 v206, v233, v92
	ds_bpermute_b32 v207, v233, v93
	s_mov_b32 s98, 0x200000
	v_lshl_add_u64 v[214:215], v[236:237], 0, s[98:99]
	s_waitcnt lgkmcnt(4)
	global_store_dwordx4 v[212:213], v[200:203], off offset:256
	v_pk_mul_f32 v[80:81], v[80:81], s[86:87] op_sel_hi:[1,0]
	v_pk_mul_f32 v[78:79], v[78:79], s[86:87] op_sel_hi:[1,0]
	v_pk_mul_f32 v[90:91], v[76:77], s[86:87] op_sel_hi:[1,0]
	v_pk_mul_f32 v[76:77], v[74:75], s[86:87] op_sel_hi:[1,0]
	v_cvt_pk_bf16_f32 v74, v82, v83
	v_cvt_pk_bf16_f32 v75, v84, v85
	v_cvt_pk_bf16_f32 v76, v76, v77
	v_cvt_pk_bf16_f32 v77, v90, v91
	ds_bpermute_b32 v208, v233, v74
	ds_bpermute_b32 v209, v233, v75
	ds_bpermute_b32 v210, v233, v76
	ds_bpermute_b32 v211, v233, v77
	s_mov_b32 s98, 0x200000
	v_lshl_add_u64 v[216:217], v[236:237], 0, s[98:99]
	s_waitcnt lgkmcnt(4)
	global_store_dwordx4 v[214:215], v[204:207], off
	v_pk_mul_f32 v[72:73], v[72:73], s[86:87] op_sel_hi:[1,0]
	v_pk_mul_f32 v[70:71], v[70:71], s[86:87] op_sel_hi:[1,0]
	v_or_b32_e32 v74, 48, v130
	v_ashrrev_i32_e32 v75, 31, v74
	v_lshlrev_b64 v[74:75], 16, v[74:75]
	v_lshl_add_u64 v[82:83], s[6:7], 0, v[74:75]
	v_pk_mul_f32 v[76:77], v[88:89], s[86:87] op_sel_hi:[1,0]
	v_pk_mul_f32 v[74:75], v[86:87], s[86:87] op_sel_hi:[1,0]
	v_pk_mul_f32 v[64:65], v[64:65], s[86:87] op_sel_hi:[1,0]
	v_cvt_pk_bf16_f32 v74, v74, v75
	v_cvt_pk_bf16_f32 v75, v76, v77
	v_cvt_pk_bf16_f32 v76, v78, v79
	v_cvt_pk_bf16_f32 v77, v80, v81
	v_lshl_add_u64 v[78:79], v[82:83], 0, v[122:123]
	ds_bpermute_b32 v200, v233, v74
	ds_bpermute_b32 v201, v233, v75
	ds_bpermute_b32 v202, v233, v76
	ds_bpermute_b32 v203, v233, v77
	s_mov_b32 s98, 0x300000
	v_lshl_add_u64 v[212:213], v[236:237], 0, s[98:99]
	s_waitcnt lgkmcnt(4)
	global_store_dwordx4 v[216:217], v[208:211], off offset:256
	v_pk_mul_f32 v[62:63], v[62:63], s[86:87] op_sel_hi:[1,0]
	v_pk_mul_f32 v[52:53], v[52:53], s[86:87] op_sel_hi:[1,0]
	v_pk_mul_f32 v[74:75], v[68:69], s[86:87] op_sel_hi:[1,0]
	v_pk_mul_f32 v[68:69], v[66:67], s[86:87] op_sel_hi:[1,0]
	v_cvt_pk_bf16_f32 v66, v70, v71
	v_cvt_pk_bf16_f32 v67, v72, v73
	v_cvt_pk_bf16_f32 v68, v68, v69
	v_cvt_pk_bf16_f32 v69, v74, v75
	ds_bpermute_b32 v204, v233, v66
	ds_bpermute_b32 v205, v233, v67
	ds_bpermute_b32 v206, v233, v68
	ds_bpermute_b32 v207, v233, v69
	s_mov_b32 s98, 0x300000
	v_lshl_add_u64 v[214:215], v[236:237], 0, s[98:99]
	s_waitcnt lgkmcnt(4)
	global_store_dwordx4 v[212:213], v[200:203], off
	v_pk_mul_f32 v[50:51], v[50:51], s[86:87] op_sel_hi:[1,0]
	v_pk_mul_f32 v[48:49], v[48:49], s[86:87] op_sel_hi:[1,0]
	v_add_u32_e32 v66, 0x80, v130
	v_ashrrev_i32_e32 v67, 31, v66
	v_lshlrev_b64 v[66:67], 16, v[66:67]
	v_lshl_add_u64 v[66:67], s[6:7], 0, v[66:67]
	v_pk_mul_f32 v[68:69], v[60:61], s[86:87] op_sel_hi:[1,0]
	v_pk_mul_f32 v[60:61], v[58:59], s[86:87] op_sel_hi:[1,0]
	v_cvt_pk_bf16_f32 v58, v62, v63
	v_cvt_pk_bf16_f32 v59, v64, v65
	v_cvt_pk_bf16_f32 v60, v60, v61
	v_cvt_pk_bf16_f32 v61, v68, v69
	v_lshl_add_u64 v[62:63], v[66:67], 0, v[122:123]
	ds_bpermute_b32 v208, v233, v58
	ds_bpermute_b32 v209, v233, v59
	ds_bpermute_b32 v210, v233, v60
	ds_bpermute_b32 v211, v233, v61
	s_mov_b32 s98, 0x800000
	v_lshl_add_u64 v[216:217], v[236:237], 0, s[98:99]
	s_waitcnt lgkmcnt(4)
	global_store_dwordx4 v[214:215], v[204:207], off offset:256
	v_pk_mul_f32 v[46:47], v[46:47], s[86:87] op_sel_hi:[1,0]
	v_pk_mul_f32 v[36:37], v[36:37], s[86:87] op_sel_hi:[1,0]
	v_pk_mul_f32 v[58:59], v[44:45], s[86:87] op_sel_hi:[1,0]
	v_pk_mul_f32 v[44:45], v[42:43], s[86:87] op_sel_hi:[1,0]
	v_cvt_pk_bf16_f32 v42, v50, v51
	v_cvt_pk_bf16_f32 v43, v52, v53
	v_cvt_pk_bf16_f32 v44, v44, v45
	v_cvt_pk_bf16_f32 v45, v58, v59
	ds_bpermute_b32 v200, v233, v42
	ds_bpermute_b32 v201, v233, v43
	ds_bpermute_b32 v202, v233, v44
	ds_bpermute_b32 v203, v233, v45
	s_mov_b32 s98, 0x800000
	v_lshl_add_u64 v[212:213], v[236:237], 0, s[98:99]
	s_waitcnt lgkmcnt(4)
	global_store_dwordx4 v[216:217], v[208:211], off
	v_pk_mul_f32 v[34:35], v[34:35], s[86:87] op_sel_hi:[1,0]
	v_pk_mul_f32 v[32:33], v[32:33], s[86:87] op_sel_hi:[1,0]
	v_add_u32_e32 v42, 0x90, v130
	v_ashrrev_i32_e32 v43, 31, v42
	v_lshlrev_b64 v[42:43], 16, v[42:43]
	v_lshl_add_u64 v[50:51], s[6:7], 0, v[42:43]
	v_pk_mul_f32 v[44:45], v[56:57], s[86:87] op_sel_hi:[1,0]
	v_pk_mul_f32 v[42:43], v[54:55], s[86:87] op_sel_hi:[1,0]
	v_pk_mul_f32 v[30:31], v[30:31], s[86:87] op_sel_hi:[1,0]
	v_cvt_pk_bf16_f32 v42, v42, v43
	v_cvt_pk_bf16_f32 v43, v44, v45
	v_cvt_pk_bf16_f32 v44, v46, v47
	v_cvt_pk_bf16_f32 v45, v48, v49
	v_lshl_add_u64 v[46:47], v[50:51], 0, v[122:123]
	ds_bpermute_b32 v204, v233, v42
	ds_bpermute_b32 v205, v233, v43
	ds_bpermute_b32 v206, v233, v44
	ds_bpermute_b32 v207, v233, v45
	s_mov_b32 s98, 0x900000
	v_lshl_add_u64 v[214:215], v[236:237], 0, s[98:99]
	s_waitcnt lgkmcnt(4)
	global_store_dwordx4 v[212:213], v[200:203], off offset:256
	v_pk_mul_f32 v[20:21], v[20:21], s[86:87] op_sel_hi:[1,0]
	v_pk_mul_f32 v[18:19], v[18:19], s[86:87] op_sel_hi:[1,0]
	v_pk_mul_f32 v[42:43], v[28:29], s[86:87] op_sel_hi:[1,0]
	v_pk_mul_f32 v[28:29], v[26:27], s[86:87] op_sel_hi:[1,0]
	v_cvt_pk_bf16_f32 v26, v34, v35
	v_cvt_pk_bf16_f32 v27, v36, v37
	v_cvt_pk_bf16_f32 v28, v28, v29
	v_cvt_pk_bf16_f32 v29, v42, v43
	ds_bpermute_b32 v208, v233, v26
	ds_bpermute_b32 v209, v233, v27
	ds_bpermute_b32 v210, v233, v28
	ds_bpermute_b32 v211, v233, v29
	s_mov_b32 s98, 0x900000
	v_lshl_add_u64 v[216:217], v[236:237], 0, s[98:99]
	s_waitcnt lgkmcnt(4)
	global_store_dwordx4 v[214:215], v[204:207], off
	v_pk_mul_f32 v[16:17], v[16:17], s[86:87] op_sel_hi:[1,0]
	v_pk_mul_f32 v[14:15], v[14:15], s[86:87] op_sel_hi:[1,0]
	v_add_u32_e32 v26, 0xa0, v130
	v_ashrrev_i32_e32 v27, 31, v26
	v_lshlrev_b64 v[26:27], 16, v[26:27]
	v_lshl_add_u64 v[34:35], s[6:7], 0, v[26:27]
	v_pk_mul_f32 v[28:29], v[40:41], s[86:87] op_sel_hi:[1,0]
	v_pk_mul_f32 v[26:27], v[38:39], s[86:87] op_sel_hi:[1,0]
	v_pk_mul_f32 v[8:9], v[8:9], s[86:87] op_sel_hi:[1,0]
	v_cvt_pk_bf16_f32 v26, v26, v27
	v_cvt_pk_bf16_f32 v27, v28, v29
	v_cvt_pk_bf16_f32 v28, v30, v31
	v_cvt_pk_bf16_f32 v29, v32, v33
	v_lshl_add_u64 v[30:31], v[34:35], 0, v[122:123]
	ds_bpermute_b32 v200, v233, v26
	ds_bpermute_b32 v201, v233, v27
	ds_bpermute_b32 v202, v233, v28
	ds_bpermute_b32 v203, v233, v29
	s_mov_b32 s98, 0xa00000
	v_lshl_add_u64 v[212:213], v[236:237], 0, s[98:99]
	s_waitcnt lgkmcnt(4)
	global_store_dwordx4 v[216:217], v[208:211], off offset:256
	v_pk_mul_f32 v[6:7], v[6:7], s[86:87] op_sel_hi:[1,0]
	s_andn2_b64 vcc, exec, s[2:3]
	v_pk_mul_f32 v[26:27], v[12:13], s[86:87] op_sel_hi:[1,0]
	v_pk_mul_f32 v[12:13], v[10:11], s[86:87] op_sel_hi:[1,0]
	v_cvt_pk_bf16_f32 v10, v18, v19
	v_cvt_pk_bf16_f32 v11, v20, v21
	v_cvt_pk_bf16_f32 v12, v12, v13
	v_cvt_pk_bf16_f32 v13, v26, v27
	ds_bpermute_b32 v204, v233, v10
	ds_bpermute_b32 v205, v233, v11
	ds_bpermute_b32 v206, v233, v12
	ds_bpermute_b32 v207, v233, v13
	s_mov_b32 s98, 0xa00000
	v_lshl_add_u64 v[214:215], v[236:237], 0, s[98:99]
	s_waitcnt lgkmcnt(4)
	global_store_dwordx4 v[212:213], v[200:203], off
	s_mov_b64 s[2:3], -1
	v_mov_b32_e32 v240, v243
	v_add_u32_e32 v10, 0xb0, v130
	v_ashrrev_i32_e32 v11, 31, v10
	v_lshlrev_b64 v[10:11], 16, v[10:11]
	v_lshl_add_u64 v[18:19], s[6:7], 0, v[10:11]
	v_pk_mul_f32 v[12:13], v[24:25], s[86:87] op_sel_hi:[1,0]
	v_pk_mul_f32 v[10:11], v[22:23], s[86:87] op_sel_hi:[1,0]
	s_nop 0
	v_cvt_pk_bf16_f32 v10, v10, v11
	v_cvt_pk_bf16_f32 v11, v12, v13
	v_cvt_pk_bf16_f32 v12, v14, v15
	v_cvt_pk_bf16_f32 v13, v16, v17
	v_lshl_add_u64 v[14:15], v[18:19], 0, v[122:123]
	ds_bpermute_b32 v208, v233, v10
	ds_bpermute_b32 v209, v233, v11
	ds_bpermute_b32 v210, v233, v12
	ds_bpermute_b32 v211, v233, v13
	s_mov_b32 s98, 0xb00000
	v_lshl_add_u64 v[216:217], v[236:237], 0, s[98:99]
	s_waitcnt lgkmcnt(4)
	global_store_dwordx4 v[214:215], v[204:207], off offset:256
	s_nop 1
	v_pk_mul_f32 v[10:11], v[4:5], s[86:87] op_sel_hi:[1,0]
	v_pk_mul_f32 v[4:5], v[2:3], s[86:87] op_sel_hi:[1,0]
	v_cvt_pk_bf16_f32 v2, v6, v7
	v_cvt_pk_bf16_f32 v3, v8, v9
	v_cvt_pk_bf16_f32 v4, v4, v5
	v_cvt_pk_bf16_f32 v5, v10, v11
	ds_bpermute_b32 v200, v233, v2
	ds_bpermute_b32 v201, v233, v3
	ds_bpermute_b32 v202, v233, v4
	ds_bpermute_b32 v203, v233, v5
	s_mov_b32 s98, 0xb00000
	v_lshl_add_u64 v[212:213], v[236:237], 0, s[98:99]
	s_waitcnt lgkmcnt(4)
	global_store_dwordx4 v[216:217], v[208:211], off
	s_waitcnt lgkmcnt(0)
	global_store_dwordx4 v[212:213], v[200:203], off offset:256
	s_cbranch_vccnz .LBB0_570
	s_andn2_b64 vcc, exec, s[4:5]
	s_cbranch_vccnz .LBB0_569
	s_barrier
	s_branch .LBB0_569

.LBB0_1246:
	s_mov_b32 s21, -1
	s_mov_b64 s[28:29], s[96:97]
	s_load_dwordx2 s[30:31], s[28:29], 0xc0
	v_mbcnt_lo_u32_b32 v0, s21, 0
	v_mbcnt_hi_u32_b32 v0, s21, v0
	v_lshrrev_b32_e32 v67, 1, v0
	v_and_or_b32 v0, v0, 15, s50
	s_waitcnt lgkmcnt(0)
	s_add_u32 s30, s30, s18
	s_addc_u32 s31, s31, s19
	s_lshl_b32 s21, s26, 7
	v_and_or_b32 v67, v67, 24, s21
	v_or_b32_e32 v146, s51, v67
	v_ashrrev_i32_e32 v67, 31, v66
	v_lshlrev_b64 v[66:67], 13, v[66:67]
	v_lshlrev_b32_e32 v68, 1, v146
	v_lshl_add_u64 v[66:67], s[30:31], 0, v[66:67]
	v_ashrrev_i32_e32 v69, 31, v68
	v_lshl_add_u64 v[66:67], v[68:69], 2, v[66:67]
	global_load_dwordx4 v[90:93], v[66:67], off
	global_load_dwordx4 v[82:85], v[66:67], off offset:16
	global_load_dwordx4 v[74:77], v[66:67], off offset:32
	s_nop 0
	global_load_dwordx4 v[66:69], v[66:67], off offset:48
	s_load_dwordx2 s[28:29], s[28:29], 0xe8
	v_ashrrev_i32_e32 v147, 31, v146
	s_andn2_b64 vcc, exec, s[2:3]
	s_mov_b64 s[2:3], -1
	s_mov_b64 s[68:69], s[94:95]
	s_waitcnt lgkmcnt(0)
	v_lshl_add_u64 v[146:147], s[28:29], 0, v[146:147]
	s_mov_b64 s[28:29], 0x72b00000
	v_lshl_add_u64 v[146:147], v[146:147], 0, s[28:29]
	v_mov_b32_e32 v240, v243
	s_waitcnt vmcnt(0)
	s_mov_b32 s99, 0
	s_mov_b32 s72, 0xc0c00000
	v_mov_b32_e32 v178, 0x41000000
	v_add_f32_e32 v91, 1.0, v91
	v_add_f32_e32 v93, 1.0, v93
	v_add_f32_e32 v83, 1.0, v83
	v_add_f32_e32 v85, 1.0, v85
	v_add_f32_e32 v75, 1.0, v75
	v_add_f32_e32 v77, 1.0, v77
	v_add_f32_e32 v67, 1.0, v67
	v_add_f32_e32 v69, 1.0, v69
	s_mov_b32 s98, -1
	v_mbcnt_lo_u32_b32 v196, s98, 0
	v_mbcnt_hi_u32_b32 v196, s98, v196
	v_and_b32_e32 v197, 3, v196
	v_lshrrev_b32_e32 v198, 2, v196
	v_lshlrev_b32_e32 v199, 4, v197
	v_or_b32_e32 v199, v199, v198
	v_lshlrev_b32_e32 v199, 2, v199
	v_lshrrev_b32_e32 v196, 4, v196
	v_sub_u32_e32 v196, v197, v196
	v_lshlrev_b32_e32 v196, 3, v196
	v_ashrrev_i32_e32 v197, 31, v196
	v_lshl_add_u64 v[196:197], v[146:147], 0, v[196:197]
	v_or_b32_e32 v176, s50, v198
	v_lshl_add_u32 v176, s62, 8, v176
	v_ashrrev_i32_e32 v177, 31, v176
	v_lshlrev_b64 v[176:177], 10, v[176:177]
	v_lshl_add_u64 v[176:177], v[196:197], 0, v[176:177]
	s_mov_b32 s98, 0x0
	v_lshl_add_u64 v[208:209], v[176:177], 0, s[98:99]
	v_fmamk_f32 v142, v142, 0x3d000000, v90
	v_fmamk_f32 v143, v143, 0x3d000000, v92
	v_fmamk_f32 v144, v144, 0x3d000000, v82
	v_fmamk_f32 v145, v145, 0x3d000000, v84
	v_min_f32_e32 v142, 0x40e00000, v142
	v_min_f32_e32 v143, 0x40e00000, v143
	v_min_f32_e32 v144, 0x40e00000, v144
	v_min_f32_e32 v145, 0x40e00000, v145
	v_mul_f32_e32 v180, 0xc01d265f, v142
	v_mul_f32_e32 v181, 0xc01d265f, v143
	v_mul_f32_e32 v182, 0xc01d265f, v144
	v_mul_f32_e32 v183, 0xc01d265f, v145
	v_exp_f32_e32 v180, v180
	v_exp_f32_e32 v181, v181
	v_exp_f32_e32 v182, v182
	v_exp_f32_e32 v183, v183
	v_fmamk_f32 v138, v138, 0x3d000000, v91
	v_fmamk_f32 v139, v139, 0x3d000000, v93
	v_fmamk_f32 v140, v140, 0x3d000000, v83
	v_fmamk_f32 v141, v141, 0x3d000000, v85
	v_add_f32_e32 v180, 1.0, v180
	v_add_f32_e32 v181, 1.0, v181
	v_add_f32_e32 v182, 1.0, v182
	v_add_f32_e32 v183, 1.0, v183
	v_rcp_f32_e32 v180, v180
	v_rcp_f32_e32 v181, v181
	v_rcp_f32_e32 v182, v182
	v_rcp_f32_e32 v183, v183
	v_med3_f32 v138, v138, s72, v178
	v_med3_f32 v139, v139, s72, v178
	v_med3_f32 v140, v140, s72, v178
	v_med3_f32 v141, v141, s72, v178
	v_mul_f32_e32 v180, v142, v180
	v_mul_f32_e32 v181, v143, v181
	v_mul_f32_e32 v182, v144, v182
	v_mul_f32_e32 v183, v145, v183
	v_mul_f32_e32 v180, v138, v180
	v_mul_f32_e32 v181, v139, v181
	v_mul_f32_e32 v182, v140, v182
	v_mul_f32_e32 v183, v141, v183
	v_cvt_pk_fp8_f32 v200, v180, v181
	v_cvt_pk_fp8_f32 v200, v182, v183 op_sel:[0,0,1]
	v_fmamk_f32 v134, v134, 0x3d000000, v74
	v_fmamk_f32 v135, v135, 0x3d000000, v76
	v_fmamk_f32 v136, v136, 0x3d000000, v66
	v_fmamk_f32 v137, v137, 0x3d000000, v68
	v_min_f32_e32 v134, 0x40e00000, v134
	v_min_f32_e32 v135, 0x40e00000, v135
	v_min_f32_e32 v136, 0x40e00000, v136
	v_min_f32_e32 v137, 0x40e00000, v137
	v_mul_f32_e32 v184, 0xc01d265f, v134
	v_mul_f32_e32 v185, 0xc01d265f, v135
	v_mul_f32_e32 v186, 0xc01d265f, v136
	v_mul_f32_e32 v187, 0xc01d265f, v137
	v_exp_f32_e32 v184, v184
	v_exp_f32_e32 v185, v185
	v_exp_f32_e32 v186, v186
	v_exp_f32_e32 v187, v187
	v_fmamk_f32 v130, v130, 0x3d000000, v75
	v_fmamk_f32 v131, v131, 0x3d000000, v77
	v_fmamk_f32 v132, v132, 0x3d000000, v67
	v_fmamk_f32 v133, v133, 0x3d000000, v69
	v_add_f32_e32 v184, 1.0, v184
	v_add_f32_e32 v185, 1.0, v185
	v_add_f32_e32 v186, 1.0, v186
	v_add_f32_e32 v187, 1.0, v187
	v_rcp_f32_e32 v184, v184
	v_rcp_f32_e32 v185, v185
	v_rcp_f32_e32 v186, v186
	v_rcp_f32_e32 v187, v187
	v_med3_f32 v130, v130, s72, v178
	v_med3_f32 v131, v131, s72, v178
	v_med3_f32 v132, v132, s72, v178
	v_med3_f32 v133, v133, s72, v178
	v_mul_f32_e32 v184, v134, v184
	v_mul_f32_e32 v185, v135, v185
	v_mul_f32_e32 v186, v136, v186
	v_mul_f32_e32 v187, v137, v187
	v_mul_f32_e32 v184, v130, v184
	v_mul_f32_e32 v185, v131, v185
	v_mul_f32_e32 v186, v132, v186
	v_mul_f32_e32 v187, v133, v187
	v_cvt_pk_fp8_f32 v201, v184, v185
	v_cvt_pk_fp8_f32 v201, v186, v187 op_sel:[0,0,1]
	ds_bpermute_b32 v200, v199, v200
	ds_bpermute_b32 v201, v199, v201
	s_mov_b32 s98, 0x4000
	v_lshl_add_u64 v[210:211], v[176:177], 0, s[98:99]
	v_fmamk_f32 v126, v126, 0x3d000000, v90
	v_fmamk_f32 v127, v127, 0x3d000000, v92
	v_fmamk_f32 v128, v128, 0x3d000000, v82
	v_fmamk_f32 v129, v129, 0x3d000000, v84
	v_min_f32_e32 v126, 0x40e00000, v126
	v_min_f32_e32 v127, 0x40e00000, v127
	v_min_f32_e32 v128, 0x40e00000, v128
	v_min_f32_e32 v129, 0x40e00000, v129
	v_mul_f32_e32 v180, 0xc01d265f, v126
	v_mul_f32_e32 v181, 0xc01d265f, v127
	v_mul_f32_e32 v182, 0xc01d265f, v128
	v_mul_f32_e32 v183, 0xc01d265f, v129
	v_exp_f32_e32 v180, v180
	v_exp_f32_e32 v181, v181
	v_exp_f32_e32 v182, v182
	v_exp_f32_e32 v183, v183
	v_fmamk_f32 v122, v122, 0x3d000000, v91
	v_fmamk_f32 v123, v123, 0x3d000000, v93
	v_fmamk_f32 v124, v124, 0x3d000000, v83
	v_fmamk_f32 v125, v125, 0x3d000000, v85
	v_add_f32_e32 v180, 1.0, v180
	v_add_f32_e32 v181, 1.0, v181
	v_add_f32_e32 v182, 1.0, v182
	v_add_f32_e32 v183, 1.0, v183
	v_rcp_f32_e32 v180, v180
	v_rcp_f32_e32 v181, v181
	v_rcp_f32_e32 v182, v182
	v_rcp_f32_e32 v183, v183
	v_med3_f32 v122, v122, s72, v178
	v_med3_f32 v123, v123, s72, v178
	v_med3_f32 v124, v124, s72, v178
	v_med3_f32 v125, v125, s72, v178
	v_mul_f32_e32 v180, v126, v180
	v_mul_f32_e32 v181, v127, v181
	v_mul_f32_e32 v182, v128, v182
	v_mul_f32_e32 v183, v129, v183
	v_mul_f32_e32 v180, v122, v180
	v_mul_f32_e32 v181, v123, v181
	v_mul_f32_e32 v182, v124, v182
	v_mul_f32_e32 v183, v125, v183
	v_cvt_pk_fp8_f32 v202, v180, v181
	v_cvt_pk_fp8_f32 v202, v182, v183 op_sel:[0,0,1]
	v_fmamk_f32 v118, v118, 0x3d000000, v74
	v_fmamk_f32 v119, v119, 0x3d000000, v76
	v_fmamk_f32 v120, v120, 0x3d000000, v66
	v_fmamk_f32 v121, v121, 0x3d000000, v68
	v_min_f32_e32 v118, 0x40e00000, v118
	v_min_f32_e32 v119, 0x40e00000, v119
	v_min_f32_e32 v120, 0x40e00000, v120
	v_min_f32_e32 v121, 0x40e00000, v121
	v_mul_f32_e32 v184, 0xc01d265f, v118
	v_mul_f32_e32 v185, 0xc01d265f, v119
	v_mul_f32_e32 v186, 0xc01d265f, v120
	v_mul_f32_e32 v187, 0xc01d265f, v121
	v_exp_f32_e32 v184, v184
	v_exp_f32_e32 v185, v185
	v_exp_f32_e32 v186, v186
	v_exp_f32_e32 v187, v187
	v_fmamk_f32 v114, v114, 0x3d000000, v75
	v_fmamk_f32 v115, v115, 0x3d000000, v77
	v_fmamk_f32 v116, v116, 0x3d000000, v67
	v_fmamk_f32 v117, v117, 0x3d000000, v69
	v_add_f32_e32 v184, 1.0, v184
	v_add_f32_e32 v185, 1.0, v185
	v_add_f32_e32 v186, 1.0, v186
	v_add_f32_e32 v187, 1.0, v187
	v_rcp_f32_e32 v184, v184
	v_rcp_f32_e32 v185, v185
	v_rcp_f32_e32 v186, v186
	v_rcp_f32_e32 v187, v187
	v_med3_f32 v114, v114, s72, v178
	v_med3_f32 v115, v115, s72, v178
	v_med3_f32 v116, v116, s72, v178
	v_med3_f32 v117, v117, s72, v178
	v_mul_f32_e32 v184, v118, v184
	v_mul_f32_e32 v185, v119, v185
	v_mul_f32_e32 v186, v120, v186
	v_mul_f32_e32 v187, v121, v187
	v_mul_f32_e32 v184, v114, v184
	v_mul_f32_e32 v185, v115, v185
	v_mul_f32_e32 v186, v116, v186
	v_mul_f32_e32 v187, v117, v187
	v_cvt_pk_fp8_f32 v203, v184, v185
	v_cvt_pk_fp8_f32 v203, v186, v187 op_sel:[0,0,1]
	ds_bpermute_b32 v202, v199, v202
	ds_bpermute_b32 v203, v199, v203
	s_waitcnt lgkmcnt(2)
	global_store_dwordx2 v[208:209], v[200:201], off
	s_mov_b32 s98, 0x8000
	v_lshl_add_u64 v[212:213], v[176:177], 0, s[98:99]
	v_fmamk_f32 v110, v110, 0x3d000000, v90
	v_fmamk_f32 v111, v111, 0x3d000000, v92
	v_fmamk_f32 v112, v112, 0x3d000000, v82
	v_fmamk_f32 v113, v113, 0x3d000000, v84
	v_min_f32_e32 v110, 0x40e00000, v110
	v_min_f32_e32 v111, 0x40e00000, v111
	v_min_f32_e32 v112, 0x40e00000, v112
	v_min_f32_e32 v113, 0x40e00000, v113
	v_mul_f32_e32 v180, 0xc01d265f, v110
	v_mul_f32_e32 v181, 0xc01d265f, v111
	v_mul_f32_e32 v182, 0xc01d265f, v112
	v_mul_f32_e32 v183, 0xc01d265f, v113
	v_exp_f32_e32 v180, v180
	v_exp_f32_e32 v181, v181
	v_exp_f32_e32 v182, v182
	v_exp_f32_e32 v183, v183
	v_fmamk_f32 v106, v106, 0x3d000000, v91
	v_fmamk_f32 v107, v107, 0x3d000000, v93
	v_fmamk_f32 v108, v108, 0x3d000000, v83
	v_fmamk_f32 v109, v109, 0x3d000000, v85
	v_add_f32_e32 v180, 1.0, v180
	v_add_f32_e32 v181, 1.0, v181
	v_add_f32_e32 v182, 1.0, v182
	v_add_f32_e32 v183, 1.0, v183
	v_rcp_f32_e32 v180, v180
	v_rcp_f32_e32 v181, v181
	v_rcp_f32_e32 v182, v182
	v_rcp_f32_e32 v183, v183
	v_med3_f32 v106, v106, s72, v178
	v_med3_f32 v107, v107, s72, v178
	v_med3_f32 v108, v108, s72, v178
	v_med3_f32 v109, v109, s72, v178
	v_mul_f32_e32 v180, v110, v180
	v_mul_f32_e32 v181, v111, v181
	v_mul_f32_e32 v182, v112, v182
	v_mul_f32_e32 v183, v113, v183
	v_mul_f32_e32 v180, v106, v180
	v_mul_f32_e32 v181, v107, v181
	v_mul_f32_e32 v182, v108, v182
	v_mul_f32_e32 v183, v109, v183
	v_cvt_pk_fp8_f32 v204, v180, v181
	v_cvt_pk_fp8_f32 v204, v182, v183 op_sel:[0,0,1]
	v_fmamk_f32 v102, v102, 0x3d000000, v74
	v_fmamk_f32 v103, v103, 0x3d000000, v76
	v_fmamk_f32 v104, v104, 0x3d000000, v66
	v_fmamk_f32 v105, v105, 0x3d000000, v68
	v_min_f32_e32 v102, 0x40e00000, v102
	v_min_f32_e32 v103, 0x40e00000, v103
	v_min_f32_e32 v104, 0x40e00000, v104
	v_min_f32_e32 v105, 0x40e00000, v105
	v_mul_f32_e32 v184, 0xc01d265f, v102
	v_mul_f32_e32 v185, 0xc01d265f, v103
	v_mul_f32_e32 v186, 0xc01d265f, v104
	v_mul_f32_e32 v187, 0xc01d265f, v105
	v_exp_f32_e32 v184, v184
	v_exp_f32_e32 v185, v185
	v_exp_f32_e32 v186, v186
	v_exp_f32_e32 v187, v187
	v_fmamk_f32 v98, v98, 0x3d000000, v75
	v_fmamk_f32 v99, v99, 0x3d000000, v77
	v_fmamk_f32 v100, v100, 0x3d000000, v67
	v_fmamk_f32 v101, v101, 0x3d000000, v69
	v_add_f32_e32 v184, 1.0, v184
	v_add_f32_e32 v185, 1.0, v185
	v_add_f32_e32 v186, 1.0, v186
	v_add_f32_e32 v187, 1.0, v187
	v_rcp_f32_e32 v184, v184
	v_rcp_f32_e32 v185, v185
	v_rcp_f32_e32 v186, v186
	v_rcp_f32_e32 v187, v187
	v_med3_f32 v98, v98, s72, v178
	v_med3_f32 v99, v99, s72, v178
	v_med3_f32 v100, v100, s72, v178
	v_med3_f32 v101, v101, s72, v178
	v_mul_f32_e32 v184, v102, v184
	v_mul_f32_e32 v185, v103, v185
	v_mul_f32_e32 v186, v104, v186
	v_mul_f32_e32 v187, v105, v187
	v_mul_f32_e32 v184, v98, v184
	v_mul_f32_e32 v185, v99, v185
	v_mul_f32_e32 v186, v100, v186
	v_mul_f32_e32 v187, v101, v187
	v_cvt_pk_fp8_f32 v205, v184, v185
	v_cvt_pk_fp8_f32 v205, v186, v187 op_sel:[0,0,1]
	ds_bpermute_b32 v204, v199, v204
	ds_bpermute_b32 v205, v199, v205
	s_waitcnt lgkmcnt(2)
	global_store_dwordx2 v[210:211], v[202:203], off
	s_mov_b32 s98, 0xc000
	v_lshl_add_u64 v[214:215], v[176:177], 0, s[98:99]
	v_fmamk_f32 v94, v94, 0x3d000000, v90
	v_fmamk_f32 v95, v95, 0x3d000000, v92
	v_fmamk_f32 v96, v96, 0x3d000000, v82
	v_fmamk_f32 v97, v97, 0x3d000000, v84
	v_min_f32_e32 v94, 0x40e00000, v94
	v_min_f32_e32 v95, 0x40e00000, v95
	v_min_f32_e32 v96, 0x40e00000, v96
	v_min_f32_e32 v97, 0x40e00000, v97
	v_mul_f32_e32 v180, 0xc01d265f, v94
	v_mul_f32_e32 v181, 0xc01d265f, v95
	v_mul_f32_e32 v182, 0xc01d265f, v96
	v_mul_f32_e32 v183, 0xc01d265f, v97
	v_exp_f32_e32 v180, v180
	v_exp_f32_e32 v181, v181
	v_exp_f32_e32 v182, v182
	v_exp_f32_e32 v183, v183
	v_fmamk_f32 v86, v86, 0x3d000000, v91
	v_fmamk_f32 v87, v87, 0x3d000000, v93
	v_fmamk_f32 v88, v88, 0x3d000000, v83
	v_fmamk_f32 v89, v89, 0x3d000000, v85
	v_add_f32_e32 v180, 1.0, v180
	v_add_f32_e32 v181, 1.0, v181
	v_add_f32_e32 v182, 1.0, v182
	v_add_f32_e32 v183, 1.0, v183
	v_rcp_f32_e32 v180, v180
	v_rcp_f32_e32 v181, v181
	v_rcp_f32_e32 v182, v182
	v_rcp_f32_e32 v183, v183
	v_med3_f32 v86, v86, s72, v178
	v_med3_f32 v87, v87, s72, v178
	v_med3_f32 v88, v88, s72, v178
	v_med3_f32 v89, v89, s72, v178
	v_mul_f32_e32 v180, v94, v180
	v_mul_f32_e32 v181, v95, v181
	v_mul_f32_e32 v182, v96, v182
	v_mul_f32_e32 v183, v97, v183
	v_mul_f32_e32 v180, v86, v180
	v_mul_f32_e32 v181, v87, v181
	v_mul_f32_e32 v182, v88, v182
	v_mul_f32_e32 v183, v89, v183
	v_cvt_pk_fp8_f32 v200, v180, v181
	v_cvt_pk_fp8_f32 v200, v182, v183 op_sel:[0,0,1]
	v_fmamk_f32 v78, v78, 0x3d000000, v74
	v_fmamk_f32 v79, v79, 0x3d000000, v76
	v_fmamk_f32 v80, v80, 0x3d000000, v66
	v_fmamk_f32 v81, v81, 0x3d000000, v68
	v_min_f32_e32 v78, 0x40e00000, v78
	v_min_f32_e32 v79, 0x40e00000, v79
	v_min_f32_e32 v80, 0x40e00000, v80
	v_min_f32_e32 v81, 0x40e00000, v81
	v_mul_f32_e32 v184, 0xc01d265f, v78
	v_mul_f32_e32 v185, 0xc01d265f, v79
	v_mul_f32_e32 v186, 0xc01d265f, v80
	v_mul_f32_e32 v187, 0xc01d265f, v81
	v_exp_f32_e32 v184, v184
	v_exp_f32_e32 v185, v185
	v_exp_f32_e32 v186, v186
	v_exp_f32_e32 v187, v187
	v_fmamk_f32 v70, v70, 0x3d000000, v75
	v_fmamk_f32 v71, v71, 0x3d000000, v77
	v_fmamk_f32 v72, v72, 0x3d000000, v67
	v_fmamk_f32 v73, v73, 0x3d000000, v69
	v_add_f32_e32 v184, 1.0, v184
	v_add_f32_e32 v185, 1.0, v185
	v_add_f32_e32 v186, 1.0, v186
	v_add_f32_e32 v187, 1.0, v187
	v_rcp_f32_e32 v184, v184
	v_rcp_f32_e32 v185, v185
	v_rcp_f32_e32 v186, v186
	v_rcp_f32_e32 v187, v187
	v_med3_f32 v70, v70, s72, v178
	v_med3_f32 v71, v71, s72, v178
	v_med3_f32 v72, v72, s72, v178
	v_med3_f32 v73, v73, s72, v178
	v_mul_f32_e32 v184, v78, v184
	v_mul_f32_e32 v185, v79, v185
	v_mul_f32_e32 v186, v80, v186
	v_mul_f32_e32 v187, v81, v187
	v_mul_f32_e32 v184, v70, v184
	v_mul_f32_e32 v185, v71, v185
	v_mul_f32_e32 v186, v72, v186
	v_mul_f32_e32 v187, v73, v187
	v_cvt_pk_fp8_f32 v201, v184, v185
	v_cvt_pk_fp8_f32 v201, v186, v187 op_sel:[0,0,1]
	ds_bpermute_b32 v200, v199, v200
	ds_bpermute_b32 v201, v199, v201
	s_waitcnt lgkmcnt(2)
	global_store_dwordx2 v[212:213], v[204:205], off
	s_mov_b32 s98, 0x20000
	v_lshl_add_u64 v[208:209], v[176:177], 0, s[98:99]
	v_fmamk_f32 v62, v62, 0x3d000000, v90
	v_fmamk_f32 v63, v63, 0x3d000000, v92
	v_fmamk_f32 v64, v64, 0x3d000000, v82
	v_fmamk_f32 v65, v65, 0x3d000000, v84
	v_min_f32_e32 v62, 0x40e00000, v62
	v_min_f32_e32 v63, 0x40e00000, v63
	v_min_f32_e32 v64, 0x40e00000, v64
	v_min_f32_e32 v65, 0x40e00000, v65
	v_mul_f32_e32 v180, 0xc01d265f, v62
	v_mul_f32_e32 v181, 0xc01d265f, v63
	v_mul_f32_e32 v182, 0xc01d265f, v64
	v_mul_f32_e32 v183, 0xc01d265f, v65
	v_exp_f32_e32 v180, v180
	v_exp_f32_e32 v181, v181
	v_exp_f32_e32 v182, v182
	v_exp_f32_e32 v183, v183
	v_fmamk_f32 v58, v58, 0x3d000000, v91
	v_fmamk_f32 v59, v59, 0x3d000000, v93
	v_fmamk_f32 v60, v60, 0x3d000000, v83
	v_fmamk_f32 v61, v61, 0x3d000000, v85
	v_add_f32_e32 v180, 1.0, v180
	v_add_f32_e32 v181, 1.0, v181
	v_add_f32_e32 v182, 1.0, v182
	v_add_f32_e32 v183, 1.0, v183
	v_rcp_f32_e32 v180, v180
	v_rcp_f32_e32 v181, v181
	v_rcp_f32_e32 v182, v182
	v_rcp_f32_e32 v183, v183
	v_med3_f32 v58, v58, s72, v178
	v_med3_f32 v59, v59, s72, v178
	v_med3_f32 v60, v60, s72, v178
	v_med3_f32 v61, v61, s72, v178
	v_mul_f32_e32 v180, v62, v180
	v_mul_f32_e32 v181, v63, v181
	v_mul_f32_e32 v182, v64, v182
	v_mul_f32_e32 v183, v65, v183
	v_mul_f32_e32 v180, v58, v180
	v_mul_f32_e32 v181, v59, v181
	v_mul_f32_e32 v182, v60, v182
	v_mul_f32_e32 v183, v61, v183
	v_cvt_pk_fp8_f32 v202, v180, v181
	v_cvt_pk_fp8_f32 v202, v182, v183 op_sel:[0,0,1]
	v_fmamk_f32 v54, v54, 0x3d000000, v74
	v_fmamk_f32 v55, v55, 0x3d000000, v76
	v_fmamk_f32 v56, v56, 0x3d000000, v66
	v_fmamk_f32 v57, v57, 0x3d000000, v68
	v_min_f32_e32 v54, 0x40e00000, v54
	v_min_f32_e32 v55, 0x40e00000, v55
	v_min_f32_e32 v56, 0x40e00000, v56
	v_min_f32_e32 v57, 0x40e00000, v57
	v_mul_f32_e32 v184, 0xc01d265f, v54
	v_mul_f32_e32 v185, 0xc01d265f, v55
	v_mul_f32_e32 v186, 0xc01d265f, v56
	v_mul_f32_e32 v187, 0xc01d265f, v57
	v_exp_f32_e32 v184, v184
	v_exp_f32_e32 v185, v185
	v_exp_f32_e32 v186, v186
	v_exp_f32_e32 v187, v187
	v_fmamk_f32 v50, v50, 0x3d000000, v75
	v_fmamk_f32 v51, v51, 0x3d000000, v77
	v_fmamk_f32 v52, v52, 0x3d000000, v67
	v_fmamk_f32 v53, v53, 0x3d000000, v69
	v_add_f32_e32 v184, 1.0, v184
	v_add_f32_e32 v185, 1.0, v185
	v_add_f32_e32 v186, 1.0, v186
	v_add_f32_e32 v187, 1.0, v187
	v_rcp_f32_e32 v184, v184
	v_rcp_f32_e32 v185, v185
	v_rcp_f32_e32 v186, v186
	v_rcp_f32_e32 v187, v187
	v_med3_f32 v50, v50, s72, v178
	v_med3_f32 v51, v51, s72, v178
	v_med3_f32 v52, v52, s72, v178
	v_med3_f32 v53, v53, s72, v178
	v_mul_f32_e32 v184, v54, v184
	v_mul_f32_e32 v185, v55, v185
	v_mul_f32_e32 v186, v56, v186
	v_mul_f32_e32 v187, v57, v187
	v_mul_f32_e32 v184, v50, v184
	v_mul_f32_e32 v185, v51, v185
	v_mul_f32_e32 v186, v52, v186
	v_mul_f32_e32 v187, v53, v187
	v_cvt_pk_fp8_f32 v203, v184, v185
	v_cvt_pk_fp8_f32 v203, v186, v187 op_sel:[0,0,1]
	ds_bpermute_b32 v202, v199, v202
	ds_bpermute_b32 v203, v199, v203
	s_waitcnt lgkmcnt(2)
	global_store_dwordx2 v[214:215], v[200:201], off
	s_mov_b32 s98, 0x24000
	v_lshl_add_u64 v[210:211], v[176:177], 0, s[98:99]
	v_fmamk_f32 v46, v46, 0x3d000000, v90
	v_fmamk_f32 v47, v47, 0x3d000000, v92
	v_fmamk_f32 v48, v48, 0x3d000000, v82
	v_fmamk_f32 v49, v49, 0x3d000000, v84
	v_min_f32_e32 v46, 0x40e00000, v46
	v_min_f32_e32 v47, 0x40e00000, v47
	v_min_f32_e32 v48, 0x40e00000, v48
	v_min_f32_e32 v49, 0x40e00000, v49
	v_mul_f32_e32 v180, 0xc01d265f, v46
	v_mul_f32_e32 v181, 0xc01d265f, v47
	v_mul_f32_e32 v182, 0xc01d265f, v48
	v_mul_f32_e32 v183, 0xc01d265f, v49
	v_exp_f32_e32 v180, v180
	v_exp_f32_e32 v181, v181
	v_exp_f32_e32 v182, v182
	v_exp_f32_e32 v183, v183
	v_fmamk_f32 v42, v42, 0x3d000000, v91
	v_fmamk_f32 v43, v43, 0x3d000000, v93
	v_fmamk_f32 v44, v44, 0x3d000000, v83
	v_fmamk_f32 v45, v45, 0x3d000000, v85
	v_add_f32_e32 v180, 1.0, v180
	v_add_f32_e32 v181, 1.0, v181
	v_add_f32_e32 v182, 1.0, v182
	v_add_f32_e32 v183, 1.0, v183
	v_rcp_f32_e32 v180, v180
	v_rcp_f32_e32 v181, v181
	v_rcp_f32_e32 v182, v182
	v_rcp_f32_e32 v183, v183
	v_med3_f32 v42, v42, s72, v178
	v_med3_f32 v43, v43, s72, v178
	v_med3_f32 v44, v44, s72, v178
	v_med3_f32 v45, v45, s72, v178
	v_mul_f32_e32 v180, v46, v180
	v_mul_f32_e32 v181, v47, v181
	v_mul_f32_e32 v182, v48, v182
	v_mul_f32_e32 v183, v49, v183
	v_mul_f32_e32 v180, v42, v180
	v_mul_f32_e32 v181, v43, v181
	v_mul_f32_e32 v182, v44, v182
	v_mul_f32_e32 v183, v45, v183
	v_cvt_pk_fp8_f32 v204, v180, v181
	v_cvt_pk_fp8_f32 v204, v182, v183 op_sel:[0,0,1]
	v_fmamk_f32 v38, v38, 0x3d000000, v74
	v_fmamk_f32 v39, v39, 0x3d000000, v76
	v_fmamk_f32 v40, v40, 0x3d000000, v66
	v_fmamk_f32 v41, v41, 0x3d000000, v68
	v_min_f32_e32 v38, 0x40e00000, v38
	v_min_f32_e32 v39, 0x40e00000, v39
	v_min_f32_e32 v40, 0x40e00000, v40
	v_min_f32_e32 v41, 0x40e00000, v41
	v_mul_f32_e32 v184, 0xc01d265f, v38
	v_mul_f32_e32 v185, 0xc01d265f, v39
	v_mul_f32_e32 v186, 0xc01d265f, v40
	v_mul_f32_e32 v187, 0xc01d265f, v41
	v_exp_f32_e32 v184, v184
	v_exp_f32_e32 v185, v185
	v_exp_f32_e32 v186, v186
	v_exp_f32_e32 v187, v187
	v_fmamk_f32 v34, v34, 0x3d000000, v75
	v_fmamk_f32 v35, v35, 0x3d000000, v77
	v_fmamk_f32 v36, v36, 0x3d000000, v67
	v_fmamk_f32 v37, v37, 0x3d000000, v69
	v_add_f32_e32 v184, 1.0, v184
	v_add_f32_e32 v185, 1.0, v185
	v_add_f32_e32 v186, 1.0, v186
	v_add_f32_e32 v187, 1.0, v187
	v_rcp_f32_e32 v184, v184
	v_rcp_f32_e32 v185, v185
	v_rcp_f32_e32 v186, v186
	v_rcp_f32_e32 v187, v187
	v_med3_f32 v34, v34, s72, v178
	v_med3_f32 v35, v35, s72, v178
	v_med3_f32 v36, v36, s72, v178
	v_med3_f32 v37, v37, s72, v178
	v_mul_f32_e32 v184, v38, v184
	v_mul_f32_e32 v185, v39, v185
	v_mul_f32_e32 v186, v40, v186
	v_mul_f32_e32 v187, v41, v187
	v_mul_f32_e32 v184, v34, v184
	v_mul_f32_e32 v185, v35, v185
	v_mul_f32_e32 v186, v36, v186
	v_mul_f32_e32 v187, v37, v187
	v_cvt_pk_fp8_f32 v205, v184, v185
	v_cvt_pk_fp8_f32 v205, v186, v187 op_sel:[0,0,1]
	ds_bpermute_b32 v204, v199, v204
	ds_bpermute_b32 v205, v199, v205
	s_waitcnt lgkmcnt(2)
	global_store_dwordx2 v[208:209], v[202:203], off
	s_mov_b32 s98, 0x28000
	v_lshl_add_u64 v[212:213], v[176:177], 0, s[98:99]
	v_fmamk_f32 v30, v30, 0x3d000000, v90
	v_fmamk_f32 v31, v31, 0x3d000000, v92
	v_fmamk_f32 v32, v32, 0x3d000000, v82
	v_fmamk_f32 v33, v33, 0x3d000000, v84
	v_min_f32_e32 v30, 0x40e00000, v30
	v_min_f32_e32 v31, 0x40e00000, v31
	v_min_f32_e32 v32, 0x40e00000, v32
	v_min_f32_e32 v33, 0x40e00000, v33
	v_mul_f32_e32 v180, 0xc01d265f, v30
	v_mul_f32_e32 v181, 0xc01d265f, v31
	v_mul_f32_e32 v182, 0xc01d265f, v32
	v_mul_f32_e32 v183, 0xc01d265f, v33
	v_exp_f32_e32 v180, v180
	v_exp_f32_e32 v181, v181
	v_exp_f32_e32 v182, v182
	v_exp_f32_e32 v183, v183
	v_fmamk_f32 v26, v26, 0x3d000000, v91
	v_fmamk_f32 v27, v27, 0x3d000000, v93
	v_fmamk_f32 v28, v28, 0x3d000000, v83
	v_fmamk_f32 v29, v29, 0x3d000000, v85
	v_add_f32_e32 v180, 1.0, v180
	v_add_f32_e32 v181, 1.0, v181
	v_add_f32_e32 v182, 1.0, v182
	v_add_f32_e32 v183, 1.0, v183
	v_rcp_f32_e32 v180, v180
	v_rcp_f32_e32 v181, v181
	v_rcp_f32_e32 v182, v182
	v_rcp_f32_e32 v183, v183
	v_med3_f32 v26, v26, s72, v178
	v_med3_f32 v27, v27, s72, v178
	v_med3_f32 v28, v28, s72, v178
	v_med3_f32 v29, v29, s72, v178
	v_mul_f32_e32 v180, v30, v180
	v_mul_f32_e32 v181, v31, v181
	v_mul_f32_e32 v182, v32, v182
	v_mul_f32_e32 v183, v33, v183
	v_mul_f32_e32 v180, v26, v180
	v_mul_f32_e32 v181, v27, v181
	v_mul_f32_e32 v182, v28, v182
	v_mul_f32_e32 v183, v29, v183
	v_cvt_pk_fp8_f32 v200, v180, v181
	v_cvt_pk_fp8_f32 v200, v182, v183 op_sel:[0,0,1]
	v_fmamk_f32 v22, v22, 0x3d000000, v74
	v_fmamk_f32 v23, v23, 0x3d000000, v76
	v_fmamk_f32 v24, v24, 0x3d000000, v66
	v_fmamk_f32 v25, v25, 0x3d000000, v68
	v_min_f32_e32 v22, 0x40e00000, v22
	v_min_f32_e32 v23, 0x40e00000, v23
	v_min_f32_e32 v24, 0x40e00000, v24
	v_min_f32_e32 v25, 0x40e00000, v25
	v_mul_f32_e32 v184, 0xc01d265f, v22
	v_mul_f32_e32 v185, 0xc01d265f, v23
	v_mul_f32_e32 v186, 0xc01d265f, v24
	v_mul_f32_e32 v187, 0xc01d265f, v25
	v_exp_f32_e32 v184, v184
	v_exp_f32_e32 v185, v185
	v_exp_f32_e32 v186, v186
	v_exp_f32_e32 v187, v187
	v_fmamk_f32 v18, v18, 0x3d000000, v75
	v_fmamk_f32 v19, v19, 0x3d000000, v77
	v_fmamk_f32 v20, v20, 0x3d000000, v67
	v_fmamk_f32 v21, v21, 0x3d000000, v69
	v_add_f32_e32 v184, 1.0, v184
	v_add_f32_e32 v185, 1.0, v185
	v_add_f32_e32 v186, 1.0, v186
	v_add_f32_e32 v187, 1.0, v187
	v_rcp_f32_e32 v184, v184
	v_rcp_f32_e32 v185, v185
	v_rcp_f32_e32 v186, v186
	v_rcp_f32_e32 v187, v187
	v_med3_f32 v18, v18, s72, v178
	v_med3_f32 v19, v19, s72, v178
	v_med3_f32 v20, v20, s72, v178
	v_med3_f32 v21, v21, s72, v178
	v_mul_f32_e32 v184, v22, v184
	v_mul_f32_e32 v185, v23, v185
	v_mul_f32_e32 v186, v24, v186
	v_mul_f32_e32 v187, v25, v187
	v_mul_f32_e32 v184, v18, v184
	v_mul_f32_e32 v185, v19, v185
	v_mul_f32_e32 v186, v20, v186
	v_mul_f32_e32 v187, v21, v187
	v_cvt_pk_fp8_f32 v201, v184, v185
	v_cvt_pk_fp8_f32 v201, v186, v187 op_sel:[0,0,1]
	ds_bpermute_b32 v200, v199, v200
	ds_bpermute_b32 v201, v199, v201
	s_waitcnt lgkmcnt(2)
	global_store_dwordx2 v[210:211], v[204:205], off
	s_mov_b32 s98, 0x2c000
	v_lshl_add_u64 v[214:215], v[176:177], 0, s[98:99]
	v_fmamk_f32 v14, v14, 0x3d000000, v90
	v_fmamk_f32 v15, v15, 0x3d000000, v92
	v_fmamk_f32 v16, v16, 0x3d000000, v82
	v_fmamk_f32 v17, v17, 0x3d000000, v84
	v_min_f32_e32 v14, 0x40e00000, v14
	v_min_f32_e32 v15, 0x40e00000, v15
	v_min_f32_e32 v16, 0x40e00000, v16
	v_min_f32_e32 v17, 0x40e00000, v17
	v_mul_f32_e32 v180, 0xc01d265f, v14
	v_mul_f32_e32 v181, 0xc01d265f, v15
	v_mul_f32_e32 v182, 0xc01d265f, v16
	v_mul_f32_e32 v183, 0xc01d265f, v17
	v_exp_f32_e32 v180, v180
	v_exp_f32_e32 v181, v181
	v_exp_f32_e32 v182, v182
	v_exp_f32_e32 v183, v183
	v_fmamk_f32 v10, v10, 0x3d000000, v91
	v_fmamk_f32 v11, v11, 0x3d000000, v93
	v_fmamk_f32 v12, v12, 0x3d000000, v83
	v_fmamk_f32 v13, v13, 0x3d000000, v85
	v_add_f32_e32 v180, 1.0, v180
	v_add_f32_e32 v181, 1.0, v181
	v_add_f32_e32 v182, 1.0, v182
	v_add_f32_e32 v183, 1.0, v183
	v_rcp_f32_e32 v180, v180
	v_rcp_f32_e32 v181, v181
	v_rcp_f32_e32 v182, v182
	v_rcp_f32_e32 v183, v183
	v_med3_f32 v10, v10, s72, v178
	v_med3_f32 v11, v11, s72, v178
	v_med3_f32 v12, v12, s72, v178
	v_med3_f32 v13, v13, s72, v178
	v_mul_f32_e32 v180, v14, v180
	v_mul_f32_e32 v181, v15, v181
	v_mul_f32_e32 v182, v16, v182
	v_mul_f32_e32 v183, v17, v183
	v_mul_f32_e32 v180, v10, v180
	v_mul_f32_e32 v181, v11, v181
	v_mul_f32_e32 v182, v12, v182
	v_mul_f32_e32 v183, v13, v183
	v_cvt_pk_fp8_f32 v202, v180, v181
	v_cvt_pk_fp8_f32 v202, v182, v183 op_sel:[0,0,1]
	v_fmamk_f32 v6, v6, 0x3d000000, v74
	v_fmamk_f32 v7, v7, 0x3d000000, v76
	v_fmamk_f32 v8, v8, 0x3d000000, v66
	v_fmamk_f32 v9, v9, 0x3d000000, v68
	v_min_f32_e32 v6, 0x40e00000, v6
	v_min_f32_e32 v7, 0x40e00000, v7
	v_min_f32_e32 v8, 0x40e00000, v8
	v_min_f32_e32 v9, 0x40e00000, v9
	v_mul_f32_e32 v184, 0xc01d265f, v6
	v_mul_f32_e32 v185, 0xc01d265f, v7
	v_mul_f32_e32 v186, 0xc01d265f, v8
	v_mul_f32_e32 v187, 0xc01d265f, v9
	v_exp_f32_e32 v184, v184
	v_exp_f32_e32 v185, v185
	v_exp_f32_e32 v186, v186
	v_exp_f32_e32 v187, v187
	v_fmamk_f32 v2, v2, 0x3d000000, v75
	v_fmamk_f32 v3, v3, 0x3d000000, v77
	v_fmamk_f32 v4, v4, 0x3d000000, v67
	v_fmamk_f32 v5, v5, 0x3d000000, v69
	v_add_f32_e32 v184, 1.0, v184
	v_add_f32_e32 v185, 1.0, v185
	v_add_f32_e32 v186, 1.0, v186
	v_add_f32_e32 v187, 1.0, v187
	v_rcp_f32_e32 v184, v184
	v_rcp_f32_e32 v185, v185
	v_rcp_f32_e32 v186, v186
	v_rcp_f32_e32 v187, v187
	v_med3_f32 v2, v2, s72, v178
	v_med3_f32 v3, v3, s72, v178
	v_med3_f32 v4, v4, s72, v178
	v_med3_f32 v5, v5, s72, v178
	v_mul_f32_e32 v184, v6, v184
	v_mul_f32_e32 v185, v7, v185
	v_mul_f32_e32 v186, v8, v186
	v_mul_f32_e32 v187, v9, v187
	v_mul_f32_e32 v184, v2, v184
	v_mul_f32_e32 v185, v3, v185
	v_mul_f32_e32 v186, v4, v186
	v_mul_f32_e32 v187, v5, v187
	v_cvt_pk_fp8_f32 v203, v184, v185
	v_cvt_pk_fp8_f32 v203, v186, v187 op_sel:[0,0,1]
	ds_bpermute_b32 v202, v199, v202
	ds_bpermute_b32 v203, v199, v203
	s_waitcnt lgkmcnt(2)
	global_store_dwordx2 v[212:213], v[200:201], off
	s_waitcnt lgkmcnt(0)
	global_store_dwordx2 v[214:215], v[202:203], off
	s_cbranch_vccnz .LBB0_1239
	s_andn2_b64 vcc, exec, s[10:11]
	s_cbranch_vccnz .LBB0_1238
	s_barrier
	s_branch .LBB0_1238

.LBB0_1352:
	s_mov_b32 s13, -1
	s_mov_b64 s[26:27], s[96:97]
	s_load_dwordx2 s[28:29], s[26:27], 0xd0
	v_mbcnt_lo_u32_b32 v0, s13, 0
	v_mbcnt_hi_u32_b32 v0, s13, v0
	v_lshrrev_b32_e32 v132, 1, v0
	v_ashrrev_i32_e32 v131, 31, v130
	s_waitcnt lgkmcnt(0)
	s_add_u32 s28, s28, s10
	s_addc_u32 s29, s29, s11
	s_lshl_b32 s13, s24, 8
	v_and_or_b32 v132, v132, 24, s13
	v_lshlrev_b64 v[130:131], 12, v[130:131]
	v_or_b32_e32 v138, s53, v132
	v_lshl_add_u64 v[130:131], s[28:29], 0, v[130:131]
	v_ashrrev_i32_e32 v139, 31, v138
	v_lshl_add_u64 v[142:143], v[138:139], 2, v[130:131]
	global_load_dwordx4 v[134:137], v[142:143], off
	global_load_dwordx4 v[130:133], v[142:143], off offset:16
	s_load_dwordx2 s[26:27], s[26:27], 0xe8
	v_and_or_b32 v0, v0, 15, s52
	v_lshl_add_u32 v172, s22, 8, v0
	v_or_b32_e32 v140, 16, v172
	v_or_b32_e32 v144, 32, v172
	v_add_u32_e32 v158, 0x80, v172
	v_ashrrev_i32_e32 v141, 31, v140
	v_ashrrev_i32_e32 v145, 31, v144
	v_ashrrev_i32_e32 v159, 31, v158
	v_lshlrev_b64 v[162:163], 10, v[140:141]
	v_lshlrev_b64 v[164:165], 10, v[144:145]
	v_lshlrev_b64 v[176:177], 10, v[158:159]
	s_waitcnt lgkmcnt(0)
	v_lshl_add_u64 v[158:159], s[26:27], 0, v[138:139]
	global_load_dwordx4 v[138:141], v[142:143], off offset:528
	s_nop 0
	global_load_dwordx4 v[142:145], v[142:143], off offset:512
	v_mov_b32_e32 v157, v1
	v_mov_b32_e32 v148, v1
	v_mov_b32_e32 v149, v1
	v_mov_b32_e32 v150, v1
	v_mov_b32_e32 v151, v1
	v_mov_b32_e32 v152, v1
	v_mov_b32_e32 v153, v1
	v_mov_b32_e32 v154, v1
	v_mov_b32_e32 v155, v1
	v_mov_b32_e32 v156, v1
	v_or_b32_e32 v146, 48, v172
	v_add_u32_e32 v174, 0x90, v172
	v_ashrrev_i32_e32 v173, 31, v172
	v_ashrrev_i32_e32 v147, 31, v146
	v_ashrrev_i32_e32 v175, 31, v174
	v_lshlrev_b64 v[160:161], 10, v[172:173]
	v_lshlrev_b64 v[146:147], 10, v[146:147]
	v_lshl_add_u64 v[178:179], v[158:159], 0, s[80:81]
	v_lshl_add_u64 v[160:161], v[178:179], 0, v[160:161]
	v_lshl_add_u64 v[158:159], v[178:179], 0, v[146:147]
	v_lshl_add_u64 v[146:147], v[178:179], 0, v[176:177]
	s_andn2_b64 vcc, exec, s[2:3]
	s_mov_b64 s[2:3], -1
	s_mov_b32 s68, s94
	v_lshl_add_u64 v[162:163], v[178:179], 0, v[162:163]
	v_lshl_add_u64 v[164:165], v[178:179], 0, v[164:165]
	s_waitcnt vmcnt(0)
	v_pk_fma_f32 v[86:87], v[86:87], s[86:87], v[134:135] op_sel_hi:[1,0,1]
	v_pk_fma_f32 v[90:91], v[90:91], s[86:87], v[130:131] op_sel_hi:[1,0,1]
	v_pk_fma_f32 v[78:79], v[78:79], s[86:87], v[134:135] op_sel_hi:[1,0,1]
	v_cvt_pk_fp8_f32 v157, v90, v91
	v_mov_b32_e32 v90, v1
	v_cvt_pk_fp8_f32 v90, v86, v87
	v_mov_b32_e32 v86, v1
	v_cvt_pk_fp8_f32 v86, v78, v79
	v_pk_fma_f32 v[58:59], v[58:59], s[86:87], v[130:131] op_sel_hi:[1,0,1]
	v_mov_b32_e32 v79, v1
	v_cvt_pk_fp8_f32 v79, v58, v59
	v_pk_fma_f32 v[66:67], v[66:67], s[86:87], v[134:135] op_sel_hi:[1,0,1]
	v_mov_b32_e32 v78, v1
	v_pk_fma_f32 v[60:61], v[60:61], s[86:87], v[132:133] op_sel_hi:[1,0,1]
	v_cvt_pk_fp8_f32 v78, v66, v67
	v_cvt_pk_fp8_f32 v79, v60, v61 op_sel:[0,0,1]
	v_pk_fma_f32 v[60:61], v[70:71], s[86:87], v[142:143] op_sel_hi:[1,0,1]
	v_mov_b32_e32 v66, v1
	v_cvt_pk_fp8_f32 v66, v60, v61
	v_pk_fma_f32 v[60:61], v[72:73], s[86:87], v[144:145] op_sel_hi:[1,0,1]
	v_pk_fma_f32 v[54:55], v[54:55], s[86:87], v[142:143] op_sel_hi:[1,0,1]
	v_pk_fma_f32 v[50:51], v[50:51], s[86:87], v[138:139] op_sel_hi:[1,0,1]
	v_cvt_pk_fp8_f32 v66, v60, v61 op_sel:[0,0,1]
	v_mov_b32_e32 v60, v1
	v_cvt_pk_fp8_f32 v60, v54, v55
	v_mov_b32_e32 v61, v1
	v_cvt_pk_fp8_f32 v61, v50, v51
	v_pk_fma_f32 v[50:51], v[56:57], s[86:87], v[144:145] op_sel_hi:[1,0,1]
	v_pk_fma_f32 v[46:47], v[46:47], s[86:87], v[142:143] op_sel_hi:[1,0,1]
	v_cvt_pk_fp8_f32 v60, v50, v51 op_sel:[0,0,1]
	v_mov_b32_e32 v50, v1
	v_cvt_pk_fp8_f32 v50, v46, v47
	v_pk_fma_f32 v[42:43], v[42:43], s[86:87], v[138:139] op_sel_hi:[1,0,1]
	v_mov_b32_e32 v51, v1
	v_cvt_pk_fp8_f32 v51, v42, v43
	v_pk_fma_f32 v[42:43], v[48:49], s[86:87], v[144:145] op_sel_hi:[1,0,1]
	v_pk_fma_f32 v[38:39], v[38:39], s[86:87], v[142:143] op_sel_hi:[1,0,1]
	v_cvt_pk_fp8_f32 v50, v42, v43 op_sel:[0,0,1]
	v_mov_b32_e32 v42, v1
	v_cvt_pk_fp8_f32 v42, v38, v39
	v_pk_fma_f32 v[34:35], v[34:35], s[86:87], v[138:139] op_sel_hi:[1,0,1]
	v_mov_b32_e32 v43, v1
	v_cvt_pk_fp8_f32 v43, v34, v35
	v_pk_fma_f32 v[34:35], v[40:41], s[86:87], v[144:145] op_sel_hi:[1,0,1]
	v_pk_fma_f32 v[30:31], v[30:31], s[86:87], v[142:143] op_sel_hi:[1,0,1]
	v_cvt_pk_fp8_f32 v42, v34, v35 op_sel:[0,0,1]
	v_mov_b32_e32 v34, v1
	v_cvt_pk_fp8_f32 v34, v30, v31
	v_pk_fma_f32 v[26:27], v[26:27], s[86:87], v[138:139] op_sel_hi:[1,0,1]
	v_mov_b32_e32 v35, v1
	v_cvt_pk_fp8_f32 v35, v26, v27
	v_pk_fma_f32 v[26:27], v[32:33], s[86:87], v[144:145] op_sel_hi:[1,0,1]
	v_pk_fma_f32 v[22:23], v[22:23], s[86:87], v[142:143] op_sel_hi:[1,0,1]
	v_cvt_pk_fp8_f32 v34, v26, v27 op_sel:[0,0,1]
	v_mov_b32_e32 v26, v1
	v_cvt_pk_fp8_f32 v26, v22, v23
	v_pk_fma_f32 v[18:19], v[18:19], s[86:87], v[138:139] op_sel_hi:[1,0,1]
	v_mov_b32_e32 v27, v1
	v_cvt_pk_fp8_f32 v27, v18, v19
	v_pk_fma_f32 v[18:19], v[24:25], s[86:87], v[144:145] op_sel_hi:[1,0,1]
	v_pk_fma_f32 v[14:15], v[14:15], s[86:87], v[142:143] op_sel_hi:[1,0,1]
	v_cvt_pk_fp8_f32 v26, v18, v19 op_sel:[0,0,1]
	v_mov_b32_e32 v18, v1
	v_cvt_pk_fp8_f32 v18, v14, v15
	v_pk_fma_f32 v[126:127], v[126:127], s[86:87], v[134:135] op_sel_hi:[1,0,1]
	v_pk_fma_f32 v[122:123], v[122:123], s[86:87], v[130:131] op_sel_hi:[1,0,1]
	v_pk_fma_f32 v[82:83], v[82:83], s[86:87], v[130:131] op_sel_hi:[1,0,1]
	v_mov_b32_e32 v91, v1
	v_pk_fma_f32 v[74:75], v[74:75], s[86:87], v[130:131] op_sel_hi:[1,0,1]
	v_mov_b32_e32 v87, v1
	v_pk_fma_f32 v[62:63], v[62:63], s[86:87], v[138:139] op_sel_hi:[1,0,1]
	v_mov_b32_e32 v67, v1
	v_pk_fma_f32 v[118:119], v[118:119], s[86:87], v[134:135] op_sel_hi:[1,0,1]
	v_pk_fma_f32 v[114:115], v[114:115], s[86:87], v[130:131] op_sel_hi:[1,0,1]
	v_cvt_pk_fp8_f32 v148, v126, v127
	v_cvt_pk_fp8_f32 v149, v122, v123
	v_cvt_pk_fp8_f32 v91, v82, v83
	v_cvt_pk_fp8_f32 v87, v74, v75
	v_cvt_pk_fp8_f32 v67, v62, v63
	v_pk_fma_f32 v[10:11], v[10:11], s[86:87], v[138:139] op_sel_hi:[1,0,1]
	v_mov_b32_e32 v19, v1
	v_pk_fma_f32 v[110:111], v[110:111], s[86:87], v[134:135] op_sel_hi:[1,0,1]
	v_pk_fma_f32 v[106:107], v[106:107], s[86:87], v[130:131] op_sel_hi:[1,0,1]
	v_cvt_pk_fp8_f32 v150, v118, v119
	v_cvt_pk_fp8_f32 v151, v114, v115
	v_cvt_pk_fp8_f32 v19, v10, v11
	v_pk_fma_f32 v[10:11], v[16:17], s[86:87], v[144:145] op_sel_hi:[1,0,1]
	v_pk_fma_f32 v[102:103], v[102:103], s[86:87], v[134:135] op_sel_hi:[1,0,1]
	v_pk_fma_f32 v[98:99], v[98:99], s[86:87], v[130:131] op_sel_hi:[1,0,1]
	v_cvt_pk_fp8_f32 v152, v110, v111
	v_cvt_pk_fp8_f32 v153, v106, v107
	v_cvt_pk_fp8_f32 v18, v10, v11 op_sel:[0,0,1]
	v_pk_fma_f32 v[6:7], v[6:7], s[86:87], v[142:143] op_sel_hi:[1,0,1]
	v_pk_fma_f32 v[2:3], v[2:3], s[86:87], v[138:139] op_sel_hi:[1,0,1]
	v_mov_b32_e32 v10, v1
	v_mov_b32_e32 v11, v1
	v_pk_fma_f32 v[128:129], v[128:129], s[86:87], v[136:137] op_sel_hi:[1,0,1]
	v_pk_fma_f32 v[124:125], v[124:125], s[86:87], v[132:133] op_sel_hi:[1,0,1]
	v_pk_fma_f32 v[94:95], v[94:95], s[86:87], v[134:135] op_sel_hi:[1,0,1]
	v_cvt_pk_fp8_f32 v154, v102, v103
	v_cvt_pk_fp8_f32 v155, v98, v99
	v_pk_fma_f32 v[82:83], v[88:89], s[86:87], v[136:137] op_sel_hi:[1,0,1]
	v_pk_fma_f32 v[84:85], v[84:85], s[86:87], v[132:133] op_sel_hi:[1,0,1]
	v_pk_fma_f32 v[74:75], v[80:81], s[86:87], v[136:137] op_sel_hi:[1,0,1]
	v_pk_fma_f32 v[76:77], v[76:77], s[86:87], v[132:133] op_sel_hi:[1,0,1]
	v_pk_fma_f32 v[58:59], v[68:69], s[86:87], v[136:137] op_sel_hi:[1,0,1]
	v_pk_fma_f32 v[62:63], v[64:65], s[86:87], v[140:141] op_sel_hi:[1,0,1]
	v_pk_fma_f32 v[28:29], v[28:29], s[86:87], v[140:141] op_sel_hi:[1,0,1]
	v_cvt_pk_fp8_f32 v10, v6, v7
	v_cvt_pk_fp8_f32 v11, v2, v3
	v_pk_fma_f32 v[120:121], v[120:121], s[86:87], v[136:137] op_sel_hi:[1,0,1]
	v_pk_fma_f32 v[116:117], v[116:117], s[86:87], v[132:133] op_sel_hi:[1,0,1]
	v_cvt_pk_fp8_f32 v156, v94, v95
	v_cvt_pk_fp8_f32 v148, v128, v129 op_sel:[0,0,1]
	v_cvt_pk_fp8_f32 v149, v124, v125 op_sel:[0,0,1]
	v_cvt_pk_fp8_f32 v90, v82, v83 op_sel:[0,0,1]
	v_cvt_pk_fp8_f32 v91, v84, v85 op_sel:[0,0,1]
	v_add_u32_e32 v84, 0xa0, v172
	v_cvt_pk_fp8_f32 v86, v74, v75 op_sel:[0,0,1]
	v_cvt_pk_fp8_f32 v87, v76, v77 op_sel:[0,0,1]
	v_add_u32_e32 v76, 0xb0, v172
	v_cvt_pk_fp8_f32 v78, v58, v59 op_sel:[0,0,1]
	v_cvt_pk_fp8_f32 v67, v62, v63 op_sel:[0,0,1]
	v_pk_fma_f32 v[52:53], v[52:53], s[86:87], v[140:141] op_sel_hi:[1,0,1]
	v_cvt_pk_fp8_f32 v35, v28, v29 op_sel:[0,0,1]
	v_pk_fma_f32 v[20:21], v[20:21], s[86:87], v[140:141] op_sel_hi:[1,0,1]
	v_pk_fma_f32 v[112:113], v[112:113], s[86:87], v[136:137] op_sel_hi:[1,0,1]
	v_pk_fma_f32 v[108:109], v[108:109], s[86:87], v[132:133] op_sel_hi:[1,0,1]
	v_cvt_pk_fp8_f32 v150, v120, v121 op_sel:[0,0,1]
	v_cvt_pk_fp8_f32 v151, v116, v117 op_sel:[0,0,1]
	v_ashrrev_i32_e32 v85, 31, v84
	v_ashrrev_i32_e32 v77, 31, v76
	v_cvt_pk_fp8_f32 v61, v52, v53 op_sel:[0,0,1]
	v_pk_fma_f32 v[44:45], v[44:45], s[86:87], v[140:141] op_sel_hi:[1,0,1]
	v_cvt_pk_fp8_f32 v27, v20, v21 op_sel:[0,0,1]
	v_pk_fma_f32 v[12:13], v[12:13], s[86:87], v[140:141] op_sel_hi:[1,0,1]
	v_pk_fma_f32 v[104:105], v[104:105], s[86:87], v[136:137] op_sel_hi:[1,0,1]
	v_pk_fma_f32 v[100:101], v[100:101], s[86:87], v[132:133] op_sel_hi:[1,0,1]
	v_cvt_pk_fp8_f32 v152, v112, v113 op_sel:[0,0,1]
	v_cvt_pk_fp8_f32 v153, v108, v109 op_sel:[0,0,1]
	v_lshlrev_b64 v[82:83], 10, v[174:175]
	v_lshlrev_b64 v[74:75], 10, v[84:85]
	v_lshlrev_b64 v[58:59], 10, v[76:77]
	v_cvt_pk_fp8_f32 v51, v44, v45 op_sel:[0,0,1]
	v_pk_fma_f32 v[36:37], v[36:37], s[86:87], v[140:141] op_sel_hi:[1,0,1]
	v_cvt_pk_fp8_f32 v19, v12, v13 op_sel:[0,0,1]
	v_pk_fma_f32 v[2:3], v[8:9], s[86:87], v[144:145] op_sel_hi:[1,0,1]
	v_pk_fma_f32 v[4:5], v[4:5], s[86:87], v[140:141] op_sel_hi:[1,0,1]
	v_pk_fma_f32 v[96:97], v[96:97], s[86:87], v[136:137] op_sel_hi:[1,0,1]
	v_pk_fma_f32 v[92:93], v[92:93], s[86:87], v[132:133] op_sel_hi:[1,0,1]
	v_cvt_pk_fp8_f32 v154, v104, v105 op_sel:[0,0,1]
	v_cvt_pk_fp8_f32 v155, v100, v101 op_sel:[0,0,1]
	v_lshl_add_u64 v[82:83], v[178:179], 0, v[82:83]
	v_lshl_add_u64 v[74:75], v[178:179], 0, v[74:75]
	v_lshl_add_u64 v[58:59], v[178:179], 0, v[58:59]
	v_cvt_pk_fp8_f32 v43, v36, v37 op_sel:[0,0,1]
	v_cvt_pk_fp8_f32 v10, v2, v3 op_sel:[0,0,1]
	v_cvt_pk_fp8_f32 v11, v4, v5 op_sel:[0,0,1]
	v_cvt_pk_fp8_f32 v156, v96, v97 op_sel:[0,0,1]
	v_cvt_pk_fp8_f32 v157, v92, v93 op_sel:[0,0,1]
	s_mov_b32 s98, -1
	v_mbcnt_lo_u32_b32 v180, s98, 0
	v_mbcnt_hi_u32_b32 v180, s98, v180
	v_and_b32_e32 v181, 3, v180
	v_lshrrev_b32_e32 v182, 2, v180
	v_lshlrev_b32_e32 v183, 4, v181
	v_or_b32_e32 v183, v183, v182
	v_lshlrev_b32_e32 v183, 2, v183
	ds_bpermute_b32 v148, v183, v148
	ds_bpermute_b32 v149, v183, v149
	ds_bpermute_b32 v150, v183, v150
	ds_bpermute_b32 v151, v183, v151
	ds_bpermute_b32 v152, v183, v152
	ds_bpermute_b32 v153, v183, v153
	ds_bpermute_b32 v154, v183, v154
	ds_bpermute_b32 v155, v183, v155
	ds_bpermute_b32 v156, v183, v156
	ds_bpermute_b32 v157, v183, v157
	ds_bpermute_b32 v90, v183, v90
	ds_bpermute_b32 v91, v183, v91
	ds_bpermute_b32 v86, v183, v86
	ds_bpermute_b32 v87, v183, v87
	ds_bpermute_b32 v78, v183, v78
	ds_bpermute_b32 v79, v183, v79
	ds_bpermute_b32 v66, v183, v66
	ds_bpermute_b32 v67, v183, v67
	ds_bpermute_b32 v60, v183, v60
	ds_bpermute_b32 v61, v183, v61
	ds_bpermute_b32 v50, v183, v50
	ds_bpermute_b32 v51, v183, v51
	ds_bpermute_b32 v42, v183, v42
	ds_bpermute_b32 v43, v183, v43
	ds_bpermute_b32 v34, v183, v34
	ds_bpermute_b32 v35, v183, v35
	ds_bpermute_b32 v26, v183, v26
	ds_bpermute_b32 v27, v183, v27
	ds_bpermute_b32 v18, v183, v18
	ds_bpermute_b32 v19, v183, v19
	ds_bpermute_b32 v10, v183, v10
	ds_bpermute_b32 v11, v183, v11
	v_lshlrev_b32_e32 v184, 3, v181
	v_or_b32_e32 v184, s13, v184
	v_or_b32_e32 v184, s53, v184
	v_mov_b32_e32 v185, 0
	v_lshl_add_u64 v[184:185], s[26:27], 0, v[184:185]
	v_lshl_add_u64 v[184:185], v[184:185], 0, s[80:81]
	v_or_b32_e32 v186, s52, v182
	v_lshl_add_u32 v186, s22, 8, v186
	v_lshlrev_b32_e32 v186, 10, v186
	v_mov_b32_e32 v187, 0
	v_lshl_add_u64 v[186:187], v[184:185], 0, v[186:187]
	s_mov_b32 s99, 0
	s_mov_b32 s98, 0x0
	v_lshl_add_u64 v[190:191], v[186:187], 0, s[98:99]
	s_mov_b32 s98, 0x4000
	v_lshl_add_u64 v[192:193], v[186:187], 0, s[98:99]
	s_mov_b32 s98, 0x8000
	v_lshl_add_u64 v[194:195], v[186:187], 0, s[98:99]
	s_mov_b32 s98, 0xc000
	v_lshl_add_u64 v[196:197], v[186:187], 0, s[98:99]
	s_mov_b32 s98, 0x20000
	v_lshl_add_u64 v[198:199], v[186:187], 0, s[98:99]
	s_mov_b32 s98, 0x24000
	v_lshl_add_u64 v[200:201], v[186:187], 0, s[98:99]
	s_mov_b32 s98, 0x28000
	v_lshl_add_u64 v[202:203], v[186:187], 0, s[98:99]
	s_mov_b32 s98, 0x2c000
	v_lshl_add_u64 v[204:205], v[186:187], 0, s[98:99]
	s_waitcnt lgkmcnt(0)
	global_store_dwordx2 v[190:191], v[148:149], off
	global_store_dwordx2 v[192:193], v[150:151], off
	global_store_dwordx2 v[194:195], v[152:153], off
	global_store_dwordx2 v[196:197], v[154:155], off
	global_store_dwordx2 v[198:199], v[156:157], off
	global_store_dwordx2 v[200:201], v[90:91], off
	global_store_dwordx2 v[202:203], v[86:87], off
	global_store_dwordx2 v[204:205], v[78:79], off
	global_store_dwordx2 v[190:191], v[66:67], off offset:128
	global_store_dwordx2 v[192:193], v[60:61], off offset:128
	global_store_dwordx2 v[194:195], v[50:51], off offset:128
	global_store_dwordx2 v[196:197], v[42:43], off offset:128
	global_store_dwordx2 v[198:199], v[34:35], off offset:128
	global_store_dwordx2 v[200:201], v[26:27], off offset:128
	global_store_dwordx2 v[202:203], v[18:19], off offset:128
	global_store_dwordx2 v[204:205], v[10:11], off offset:128
	s_cbranch_vccnz .LBB0_1341
	s_andn2_b64 vcc, exec, s[6:7]
	s_cbranch_vccnz .LBB0_1340
	s_barrier
	s_branch .LBB0_1340
